# combine (last layer): final-norm gain chunks hoisted out of the row loop (no per-chunk load+drain)
# speedup vs baseline: 1.0217x; 1.0020x over previous
.LBB0_3710:
	s_cmp_lt_i32 s88, 32
	s_cselect_b64 s[2:3], -1, 0
	s_and_b64 s[4:5], s[2:3], s[6:7]
	s_andn2_b64 vcc, exec, s[4:5]
	s_cbranch_vccnz .LBB0_3714
	v_mbcnt_lo_u32_b32 v0, -1, 0
	v_mbcnt_hi_u32_b32 v1, -1, v0
	v_lshl_or_b32 v0, s96, 6, v1
	v_readlane_b32 s7, v254, 0
	s_mov_b32 s6, s7
	v_readfirstlane_b32 s4, v0
	s_ashr_i32 s5, s4, 6
	s_lshl_b32 s7, s7, 3
	s_add_i32 s16, s7, s5
	s_cmpk_gt_i32 s16, 0x7fff
	s_cbranch_scc1 .LBB0_3714
	s_waitcnt vmcnt(0)
	v_and_b32_e32 v3, 64, v1
	v_add_u32_e32 v3, 64, v3
	v_xor_b32_e32 v5, 1, v1
	s_load_dword s10, s[0:1], 0x108
	v_cmp_lt_i32_e32 vcc, v5, v3
	v_lshlrev_b32_e32 v2, 2, v0
	v_and_b32_e32 v2, 0xfc, v2
	v_cndmask_b32_e32 v5, v1, v5, vcc
	v_lshlrev_b32_e32 v32, 2, v5
	v_xor_b32_e32 v5, 2, v1
	v_cmp_lt_i32_e32 vcc, v5, v3
	s_waitcnt lgkmcnt(0)
	s_lshl_b32 s4, s10, 3
	s_add_u32 s17, s86, 0xdc0000
	v_cndmask_b32_e32 v5, v1, v5, vcc
	v_lshlrev_b32_e32 v33, 2, v5
	v_xor_b32_e32 v5, 4, v1
	v_cmp_lt_i32_e32 vcc, v5, v3
	v_mov_b32_e32 v17, 0
	s_addc_u32 s18, s87, 0
	v_cndmask_b32_e32 v5, v1, v5, vcc
	v_lshlrev_b32_e32 v16, 1, v2
	s_add_u32 s19, s86, 0xf40000
	v_lshlrev_b32_e32 v34, 2, v5
	v_xor_b32_e32 v5, 8, v1
	v_lshl_add_u64 v[10:11], s[86:87], 0, v[16:17]
	s_mov_b64 s[8:9], 0x47600000
	s_addc_u32 s20, s87, 0
	v_cmp_lt_i32_e32 vcc, v5, v3
	v_lshl_add_u64 v[18:19], v[10:11], 0, s[8:9]
	s_lshl_b32 s6, s6, 5
	s_lshl_b32 s8, s5, 2
	v_cndmask_b32_e32 v5, v1, v5, vcc
	s_add_i32 s6, s6, s8
	v_lshlrev_b32_e32 v35, 2, v5
	v_xor_b32_e32 v5, 16, v1
	s_or_b32 s6, s6, 3
	s_lshl_b32 s21, s10, 5
	s_ashr_i32 s8, s5, 31
	s_ashr_i32 s9, s7, 31
	v_cmp_lt_i32_e32 vcc, v5, v3
	s_add_u32 s10, s5, s7
	s_addc_u32 s11, s8, s9
	v_cndmask_b32_e32 v5, v1, v5, vcc
	v_lshlrev_b32_e32 v36, 2, v5
	v_xor_b32_e32 v5, 32, v1
	s_lshl_b64 s[8:9], s[10:11], 11
	v_cmp_lt_i32_e32 vcc, v5, v3
	v_and_b32_e32 v3, 63, v0
	s_add_u32 s8, s86, s8
	v_cndmask_b32_e32 v1, v1, v5, vcc
	v_lshlrev_b32_e32 v16, 3, v3
	s_addc_u32 s9, s87, s9
	v_lshlrev_b32_e32 v37, 2, v1
	v_lshl_add_u64 v[0:1], s[8:9], 0, v[16:17]
	s_mov_b64 s[8:9], 0xf100400
	s_ashr_i32 s5, s4, 31
	v_lshl_add_u64 v[20:21], v[0:1], 0, s[8:9]
	s_lshl_b64 s[8:9], s[4:5], 11
	s_lshl_b64 s[10:11], s[10:11], 12
	s_add_u32 s10, s84, s10
	v_lshlrev_b32_e32 v16, 4, v3
	s_addc_u32 s11, s85, s11
	v_or_b32_e32 v4, 0x100, v2
	v_or_b32_e32 v6, 0x200, v2
	v_or_b32_e32 v8, 0x300, v2
	v_lshl_add_u64 v[0:1], s[10:11], 0, v[16:17]
	s_mov_b64 s[10:11], 0xc00
	v_lshl_add_u64 v[22:23], v[0:1], 0, s[10:11]
	s_lshl_b64 s[10:11], s[4:5], 12
	v_lshlrev_b32_e32 v16, 2, v2
	v_lshlrev_b32_e32 v38, 2, v4
	v_lshlrev_b32_e32 v39, 2, v6
	v_lshlrev_b32_e32 v40, 2, v8
	v_mov_b32_e32 v41, 0x358637bd
	s_mov_b32 s5, 0x800000
	s_load_dwordx2 s[12:13], s[0:1], 0xe0
	s_waitcnt lgkmcnt(0)
	global_load_dwordx4 v[124:127], v16, s[12:13] offset:1024
	global_load_dwordx4 v[128:131], v16, s[12:13] offset:2048
	global_load_dwordx4 v[132:135], v16, s[12:13] offset:3072
	s_waitcnt vmcnt(0)
.LBB0_3713:
	s_ashr_i32 s7, s16, 12
	s_add_i32 s7, s7, 9
	s_mul_hi_i32 s12, s7, 0x6000
	s_mulk_i32 s7, 0x6000
	s_add_u32 s7, s86, s7
	s_addc_u32 s13, s87, s12
	s_add_u32 s12, s7, 0x505000
	s_addc_u32 s13, s13, 0
	s_add_i32 s14, s6, -3
	s_ashr_i32 s15, s14, 31
	global_load_dwordx2 v[24:25], v[20:21], off offset:-1024
	global_load_dwordx2 v[26:27], v[20:21], off offset:-512
	global_load_dwordx2 v[28:29], v[20:21], off
	global_load_dwordx2 v[30:31], v[20:21], off offset:512
	global_load_dwordx4 v[0:3], v16, s[12:13]
	global_load_dwordx4 v[4:7], v38, s[12:13]
	global_load_dwordx4 v[8:11], v39, s[12:13]
	global_load_dwordx4 v[12:15], v40, s[12:13]
	s_lshl_b64 s[12:13], s[14:15], 2
	s_add_u32 s14, s19, s12
	s_addc_u32 s15, s20, s13
	s_add_i32 s22, s6, -2
	s_ashr_i32 s23, s22, 31
	global_load_dword v42, v17, s[14:15]
	s_lshl_b64 s[14:15], s[22:23], 2
	s_add_u32 s22, s19, s14
	s_addc_u32 s23, s20, s15
	s_add_i32 s24, s6, -1
	s_ashr_i32 s25, s24, 31
	global_load_dword v44, v17, s[22:23]
	s_lshl_b64 s[22:23], s[24:25], 2
	s_add_u32 s24, s19, s22
	s_addc_u32 s25, s20, s23
	s_ashr_i32 s7, s6, 31
	global_load_dword v46, v17, s[24:25]
	s_lshl_b64 s[24:25], s[6:7], 2
	s_add_u32 s26, s19, s24
	s_addc_u32 s27, s20, s25
	global_load_dword v48, v17, s[26:27]
	s_add_u32 s12, s17, s12
	s_addc_u32 s13, s18, s13
	global_load_dword v50, v17, s[12:13]
	s_add_u32 s12, s17, s14
	s_addc_u32 s13, s18, s15
	global_load_dword v52, v17, s[12:13]
	s_add_u32 s12, s17, s22
	s_addc_u32 s13, s18, s23
	global_load_dword v54, v17, s[12:13]
	s_add_u32 s12, s17, s24
	s_addc_u32 s13, s18, s25
	global_load_dword v56, v17, s[12:13]
	s_add_i32 s16, s16, s4
	s_add_i32 s6, s6, s21
	v_lshl_add_u64 v[20:21], v[20:21], 0, s[8:9]
	s_cmp_lt_i32 s16, 0x8000
	s_waitcnt vmcnt(15)
	v_lshlrev_b32_e32 v58, 16, v24
	v_and_b32_e32 v59, 0xffff0000, v24
	v_lshlrev_b32_e32 v60, 16, v25
	v_and_b32_e32 v61, 0xffff0000, v25
	s_waitcnt vmcnt(14)
	v_lshlrev_b32_e32 v62, 16, v26
	v_and_b32_e32 v63, 0xffff0000, v26
	v_lshlrev_b32_e32 v64, 16, v27
	v_and_b32_e32 v65, 0xffff0000, v27
	s_waitcnt vmcnt(13)
	v_lshlrev_b32_e32 v66, 16, v28
	v_and_b32_e32 v67, 0xffff0000, v28
	s_waitcnt vmcnt(7)
	v_ashrrev_i32_e32 v43, 31, v42
	v_lshlrev_b64 v[24:25], 11, v[42:43]
	v_lshl_add_u64 v[24:25], v[18:19], 0, v[24:25]
	global_load_dwordx2 v[42:43], v[24:25], off
	global_load_dwordx2 v[70:71], v[24:25], off offset:512
	global_load_dwordx2 v[72:73], v[24:25], off offset:1024
	global_load_dwordx2 v[74:75], v[24:25], off offset:1536
	v_lshlrev_b32_e32 v28, 16, v29
	v_and_b32_e32 v29, 0xffff0000, v29
	s_waitcnt vmcnt(10)
	v_ashrrev_i32_e32 v45, 31, v44
	v_lshlrev_b64 v[24:25], 11, v[44:45]
	v_lshl_add_u64 v[24:25], v[18:19], 0, v[24:25]
	global_load_dwordx2 v[44:45], v[24:25], off
	global_load_dwordx2 v[76:77], v[24:25], off offset:512
	global_load_dwordx2 v[78:79], v[24:25], off offset:1024
	global_load_dwordx2 v[80:81], v[24:25], off offset:1536
	v_lshlrev_b32_e32 v68, 16, v30
	s_waitcnt vmcnt(13)
	v_ashrrev_i32_e32 v47, 31, v46
	v_lshlrev_b64 v[24:25], 11, v[46:47]
	v_lshl_add_u64 v[24:25], v[18:19], 0, v[24:25]
	global_load_dwordx2 v[46:47], v[24:25], off
	global_load_dwordx2 v[82:83], v[24:25], off offset:512
	global_load_dwordx2 v[84:85], v[24:25], off offset:1024
	global_load_dwordx2 v[86:87], v[24:25], off offset:1536
	s_waitcnt vmcnt(16)
	v_ashrrev_i32_e32 v49, 31, v48
	v_lshlrev_b64 v[24:25], 11, v[48:49]
	v_lshl_add_u64 v[24:25], v[18:19], 0, v[24:25]
	global_load_dwordx2 v[48:49], v[24:25], off
	global_load_dwordx2 v[88:89], v[24:25], off offset:512
	global_load_dwordx2 v[90:91], v[24:25], off offset:1024
	global_load_dwordx2 v[92:93], v[24:25], off offset:1536
	s_load_dwordx2 s[12:13], s[0:1], 0xe0
	s_waitcnt lgkmcnt(0)
	global_load_dwordx4 v[24:27], v16, s[12:13]
	v_and_b32_e32 v69, 0xffff0000, v30
	v_lshlrev_b32_e32 v30, 16, v31
	v_and_b32_e32 v31, 0xffff0000, v31
	s_waitcnt vmcnt(16)
	v_lshlrev_b32_e32 v94, 16, v42
	v_and_b32_e32 v95, 0xffff0000, v42
	v_lshlrev_b32_e32 v42, 16, v43
	v_and_b32_e32 v43, 0xffff0000, v43
	s_waitcnt vmcnt(15)
	v_lshlrev_b32_e32 v96, 16, v70
	v_and_b32_e32 v97, 0xffff0000, v70
	s_waitcnt vmcnt(12)
	v_lshlrev_b32_e32 v102, 16, v44
	v_and_b32_e32 v103, 0xffff0000, v44
	v_lshlrev_b32_e32 v44, 16, v45
	v_and_b32_e32 v45, 0xffff0000, v45
	s_waitcnt vmcnt(11)
	v_lshlrev_b32_e32 v104, 16, v76
	v_and_b32_e32 v105, 0xffff0000, v76
	v_lshlrev_b32_e32 v76, 16, v77
	v_and_b32_e32 v77, 0xffff0000, v77
	s_waitcnt vmcnt(10)
	v_lshlrev_b32_e32 v106, 16, v78
	v_and_b32_e32 v107, 0xffff0000, v78
	v_lshlrev_b32_e32 v78, 16, v79
	v_and_b32_e32 v79, 0xffff0000, v79
	s_waitcnt vmcnt(9)
	v_lshlrev_b32_e32 v108, 16, v80
	v_and_b32_e32 v109, 0xffff0000, v80
	v_lshlrev_b32_e32 v80, 16, v81
	v_and_b32_e32 v81, 0xffff0000, v81
	v_lshlrev_b32_e32 v70, 16, v71
	v_and_b32_e32 v71, 0xffff0000, v71
	v_lshlrev_b32_e32 v98, 16, v72
	v_and_b32_e32 v99, 0xffff0000, v72
	v_lshlrev_b32_e32 v72, 16, v73
	v_and_b32_e32 v73, 0xffff0000, v73
	v_lshlrev_b32_e32 v100, 16, v74
	v_and_b32_e32 v101, 0xffff0000, v74
	v_lshlrev_b32_e32 v74, 16, v75
	v_and_b32_e32 v75, 0xffff0000, v75
	v_pk_mul_f32 v[102:103], v[52:53], v[102:103] op_sel_hi:[0,1]
	v_pk_mul_f32 v[44:45], v[52:53], v[44:45] op_sel_hi:[0,1]
	v_pk_mul_f32 v[104:105], v[52:53], v[104:105] op_sel_hi:[0,1]
	v_pk_mul_f32 v[76:77], v[52:53], v[76:77] op_sel_hi:[0,1]
	v_pk_mul_f32 v[78:79], v[52:53], v[78:79] op_sel_hi:[0,1]
	v_pk_mul_f32 v[106:107], v[52:53], v[106:107] op_sel_hi:[0,1]
	v_pk_mul_f32 v[80:81], v[52:53], v[80:81] op_sel_hi:[0,1]
	v_pk_mul_f32 v[52:53], v[52:53], v[108:109] op_sel_hi:[0,1]
	v_pk_fma_f32 v[42:43], v[50:51], v[42:43], v[44:45] op_sel_hi:[0,1,1]
	v_pk_fma_f32 v[44:45], v[50:51], v[94:95], v[102:103] op_sel_hi:[0,1,1]
	v_pk_fma_f32 v[70:71], v[50:51], v[70:71], v[76:77] op_sel_hi:[0,1,1]
	v_pk_fma_f32 v[76:77], v[50:51], v[96:97], v[104:105] op_sel_hi:[0,1,1]
	v_pk_fma_f32 v[94:95], v[50:51], v[98:99], v[106:107] op_sel_hi:[0,1,1]
	v_pk_fma_f32 v[72:73], v[50:51], v[72:73], v[78:79] op_sel_hi:[0,1,1]
	v_pk_fma_f32 v[52:53], v[50:51], v[100:101], v[52:53] op_sel_hi:[0,1,1]
	v_pk_fma_f32 v[50:51], v[50:51], v[74:75], v[80:81] op_sel_hi:[0,1,1]
	s_waitcnt vmcnt(8)
	v_lshlrev_b32_e32 v74, 16, v46
	v_and_b32_e32 v75, 0xffff0000, v46
	v_lshlrev_b32_e32 v46, 16, v47
	v_and_b32_e32 v47, 0xffff0000, v47
	s_waitcnt vmcnt(7)
	v_lshlrev_b32_e32 v78, 16, v82
	v_and_b32_e32 v79, 0xffff0000, v82
	v_lshlrev_b32_e32 v80, 16, v83
	v_and_b32_e32 v81, 0xffff0000, v83
	s_waitcnt vmcnt(6)
	v_lshlrev_b32_e32 v82, 16, v84
	v_and_b32_e32 v83, 0xffff0000, v84
	v_lshlrev_b32_e32 v84, 16, v85
	v_and_b32_e32 v85, 0xffff0000, v85
	s_waitcnt vmcnt(5)
	v_lshlrev_b32_e32 v96, 16, v86
	v_and_b32_e32 v97, 0xffff0000, v86
	v_lshlrev_b32_e32 v86, 16, v87
	v_and_b32_e32 v87, 0xffff0000, v87
	v_pk_fma_f32 v[44:45], v[54:55], v[74:75], v[44:45] op_sel_hi:[0,1,1]
	v_pk_fma_f32 v[42:43], v[54:55], v[46:47], v[42:43] op_sel_hi:[0,1,1]
	v_pk_fma_f32 v[46:47], v[54:55], v[78:79], v[76:77] op_sel_hi:[0,1,1]
	v_pk_fma_f32 v[70:71], v[54:55], v[80:81], v[70:71] op_sel_hi:[0,1,1]
	v_pk_fma_f32 v[72:73], v[54:55], v[84:85], v[72:73] op_sel_hi:[0,1,1]
	v_pk_fma_f32 v[74:75], v[54:55], v[82:83], v[94:95] op_sel_hi:[0,1,1]
	v_pk_fma_f32 v[50:51], v[54:55], v[86:87], v[50:51] op_sel_hi:[0,1,1]
	v_pk_fma_f32 v[52:53], v[54:55], v[96:97], v[52:53] op_sel_hi:[0,1,1]
	s_waitcnt vmcnt(4)
	v_lshlrev_b32_e32 v54, 16, v48
	v_and_b32_e32 v55, 0xffff0000, v48
	v_lshlrev_b32_e32 v48, 16, v49
	v_and_b32_e32 v49, 0xffff0000, v49
	s_waitcnt vmcnt(3)
	v_lshlrev_b32_e32 v76, 16, v88
	v_and_b32_e32 v77, 0xffff0000, v88
	v_lshlrev_b32_e32 v78, 16, v89
	v_and_b32_e32 v79, 0xffff0000, v89
	s_waitcnt vmcnt(2)
	v_lshlrev_b32_e32 v82, 16, v91
	v_and_b32_e32 v83, 0xffff0000, v91
	s_waitcnt vmcnt(1)
	v_lshlrev_b32_e32 v86, 16, v93
	v_and_b32_e32 v87, 0xffff0000, v93
	v_pk_fma_f32 v[42:43], v[56:57], v[48:49], v[42:43] op_sel_hi:[0,1,1]
	v_pk_fma_f32 v[44:45], v[56:57], v[54:55], v[44:45] op_sel_hi:[0,1,1]
	v_pk_fma_f32 v[48:49], v[56:57], v[78:79], v[70:71] op_sel_hi:[0,1,1]
	v_pk_fma_f32 v[46:47], v[56:57], v[76:77], v[46:47] op_sel_hi:[0,1,1]
	v_lshlrev_b32_e32 v80, 16, v90
	v_and_b32_e32 v81, 0xffff0000, v90
	v_lshlrev_b32_e32 v84, 16, v92
	v_and_b32_e32 v85, 0xffff0000, v92
	v_pk_fma_f32 v[70:71], v[56:57], v[82:83], v[72:73] op_sel_hi:[0,1,1]
	v_pk_fma_f32 v[50:51], v[56:57], v[86:87], v[50:51] op_sel_hi:[0,1,1]
	v_pk_fma_f32 v[0:1], v[0:1], v[44:45], v[58:59]
	v_pk_fma_f32 v[2:3], v[2:3], v[42:43], v[60:61]
	v_pk_fma_f32 v[4:5], v[4:5], v[46:47], v[62:63]
	v_pk_fma_f32 v[6:7], v[6:7], v[48:49], v[64:65]
	v_pk_fma_f32 v[54:55], v[56:57], v[80:81], v[74:75] op_sel_hi:[0,1,1]
	v_pk_fma_f32 v[52:53], v[56:57], v[84:85], v[52:53] op_sel_hi:[0,1,1]
	v_pk_fma_f32 v[10:11], v[10:11], v[70:71], v[28:29]
	v_pk_fma_f32 v[14:15], v[14:15], v[50:51], v[30:31]
	v_pk_mul_f32 v[28:29], v[2:3], v[2:3]
	v_pk_mul_f32 v[30:31], v[0:1], v[0:1]
	v_pk_mul_f32 v[42:43], v[6:7], v[6:7]
	v_pk_mul_f32 v[44:45], v[4:5], v[4:5]
	v_pk_fma_f32 v[8:9], v[8:9], v[54:55], v[66:67]
	v_pk_fma_f32 v[12:13], v[12:13], v[52:53], v[68:69]
	v_pk_mov_b32 v[50:51], v[30:31], v[28:29] op_sel:[1,0]
	v_mov_b32_e32 v31, v29
	v_pk_mov_b32 v[28:29], v[44:45], v[42:43] op_sel:[1,0]
	v_mov_b32_e32 v45, v43
	v_mul_f32_e32 v49, v12, v12
	v_mul_f32_e32 v46, v9, v9
	v_mul_f32_e32 v48, v11, v11
	v_pk_add_f32 v[30:31], v[50:51], v[30:31]
	v_pk_add_f32 v[28:29], v[28:29], v[44:45]
	v_mul_f32_e32 v52, v13, v13
	v_mul_f32_e32 v53, v14, v14
	v_mul_f32_e32 v54, v15, v15
	v_pk_fma_f32 v[42:43], v[8:9], v[8:9], v[46:47] op_sel_hi:[1,1,0]
	v_pk_fma_f32 v[46:47], v[10:11], v[10:11], v[48:49] op_sel_hi:[1,1,0]
	v_pk_add_f32 v[30:31], v[30:31], v[30:31] op_sel:[0,1] op_sel_hi:[1,0]
	v_pk_add_f32 v[28:29], v[28:29], v[28:29] op_sel:[0,1] op_sel_hi:[1,0]
	v_mov_b32_e32 v43, v53
	v_mov_b32_e32 v47, v54
	v_mov_b32_e32 v31, v49
	v_mov_b32_e32 v29, v52
	v_pk_add_f32 v[42:43], v[42:43], v[46:47]
	v_pk_add_f32 v[28:29], v[30:31], v[28:29]
	s_nop 0
	v_pk_add_f32 v[28:29], v[28:29], v[42:43]
	s_nop 0
	v_add_f32_e32 v28, v28, v29
	ds_bpermute_b32 v29, v32, v28
	s_waitcnt lgkmcnt(0)
	v_add_f32_e32 v28, v28, v29
	ds_bpermute_b32 v29, v33, v28
	s_waitcnt lgkmcnt(0)
	v_add_f32_e32 v28, v28, v29
	ds_bpermute_b32 v29, v34, v28
	s_waitcnt lgkmcnt(0)
	v_add_f32_e32 v28, v28, v29
	ds_bpermute_b32 v29, v35, v28
	s_waitcnt lgkmcnt(0)
	v_add_f32_e32 v28, v28, v29
	ds_bpermute_b32 v29, v36, v28
	s_waitcnt lgkmcnt(0)
	v_add_f32_e32 v28, v28, v29
	ds_bpermute_b32 v29, v37, v28
	s_waitcnt lgkmcnt(0)
	v_add_f32_e32 v28, v28, v29
	v_fmamk_f32 v28, v28, 0x3a800000, v41
	v_mul_f32_e32 v29, 0x4b800000, v28
	v_cmp_gt_f32_e32 vcc, s5, v28
	s_nop 1
	v_cndmask_b32_e32 v28, v28, v29, vcc
	v_rsq_f32_e32 v28, v28
	s_nop 0
	v_mul_f32_e32 v29, 0x45800000, v28
	v_cndmask_b32_e32 v28, v28, v29, vcc
	v_pk_mul_f32 v[0:1], v[0:1], v[28:29] op_sel_hi:[1,0]
	v_pk_mul_f32 v[2:3], v[2:3], v[28:29] op_sel_hi:[1,0]
	s_waitcnt vmcnt(0)
	v_pk_mul_f32 v[0:1], v[24:25], v[0:1]
	v_pk_mul_f32 v[2:3], v[26:27], v[2:3]
	global_store_dwordx4 v[22:23], v[0:3], off offset:-3072
	s_load_dwordx2 s[12:13], s[0:1], 0xe0
	s_waitcnt lgkmcnt(0)
	v_pk_mul_f32 v[6:7], v[6:7], v[28:29] op_sel_hi:[1,0]
	v_pk_mul_f32 v[4:5], v[4:5], v[28:29] op_sel_hi:[1,0]
	v_pk_mul_f32 v[2:3], v[126:127], v[6:7]
	v_pk_mul_f32 v[0:1], v[124:125], v[4:5]
	global_store_dwordx4 v[22:23], v[0:3], off offset:-2048
	s_load_dwordx2 s[12:13], s[0:1], 0xe0
	s_waitcnt lgkmcnt(0)
	v_pk_mul_f32 v[4:5], v[10:11], v[28:29] op_sel_hi:[1,0]
	v_pk_mul_f32 v[6:7], v[8:9], v[28:29] op_sel_hi:[1,0]
	v_pk_mul_f32 v[2:3], v[130:131], v[4:5]
	v_pk_mul_f32 v[0:1], v[128:129], v[6:7]
	global_store_dwordx4 v[22:23], v[0:3], off offset:-1024
	s_load_dwordx2 s[12:13], s[0:1], 0xe0
	s_waitcnt lgkmcnt(0)
	v_pk_mul_f32 v[4:5], v[14:15], v[28:29] op_sel_hi:[1,0]
	v_pk_mul_f32 v[6:7], v[12:13], v[28:29] op_sel_hi:[1,0]
	v_pk_mul_f32 v[2:3], v[134:135], v[4:5]
	v_pk_mul_f32 v[0:1], v[132:133], v[6:7]
	global_store_dwordx4 v[22:23], v[0:3], off
	v_lshl_add_u64 v[22:23], v[22:23], 0, s[10:11]
	s_cbranch_scc1 .LBB0_3713
